# speedup vs baseline: 1.0397x; 1.0005x over previous
.LBB2_13:
	ds_read_b128 v[154:157], v141
	ds_read_b128 v[158:161], v141 offset:1024
	ds_read_b128 v[162:165], v141 offset:2048
	ds_read_b128 v[166:169], v141 offset:3072
	s_add_i32 s64, s38, 2
	s_cmp_eq_u32 s31, s38
	s_cselect_b32 s38, s2, s62
	s_cselect_b32 s41, s35, s37
	s_cselect_b32 s40, s34, s36
	s_cselect_b32 s39, s3, s63
	v_lshl_add_u64 v[202:203], s[36:37], 0, v[128:129]
	v_lshl_add_u64 v[204:205], v[202:203], 0, s[20:21]
	s_add_i32 m0, s43, 0xc000
	ds_read_b128 v[170:173], v143
	ds_read_b128 v[174:177], v143 offset:1024
	ds_read_b128 v[178:181], v143 offset:2048
	ds_read_b128 v[182:185], v143 offset:3072
	ds_read_b128 v[186:189], v143 offset:4096
	ds_read_b128 v[190:193], v143 offset:5120
	ds_read_b128 v[194:197], v143 offset:6144
	ds_read_b128 v[198:201], v143 offset:7168
	global_load_lds_dwordx4 v[204:205], off
	v_lshl_add_u64 v[202:203], v[202:203], 0, s[22:23]
	s_add_i32 m0, s43, 0xe000
	s_nop 0
	global_load_lds_dwordx4 v[202:203], off
	s_waitcnt lgkmcnt(8)
	s_barrier
	s_waitcnt lgkmcnt(0)
	s_setprio 1
	s_waitcnt lgkmcnt(0)
	v_mfma_f32_16x16x32_f16 v[120:123], v[154:157], v[170:173], v[120:123]
	v_mfma_f32_16x16x32_f16 v[124:127], v[162:165], v[170:173], v[124:127]
	v_mfma_f32_16x16x32_f16 v[104:107], v[154:157], v[178:181], v[104:107]
	v_mfma_f32_16x16x32_f16 v[108:111], v[162:165], v[178:181], v[108:111]
	v_mfma_f32_16x16x32_f16 v[88:91], v[154:157], v[186:189], v[88:91]
	v_mfma_f32_16x16x32_f16 v[92:95], v[162:165], v[186:189], v[92:95]
	v_mfma_f32_16x16x32_f16 v[72:75], v[154:157], v[194:197], v[72:75]
	v_mfma_f32_16x16x32_f16 v[76:79], v[162:165], v[194:197], v[76:79]
	v_mfma_f32_16x16x32_f16 v[120:123], v[158:161], v[174:177], v[120:123]
	v_mfma_f32_16x16x32_f16 v[124:127], v[166:169], v[174:177], v[124:127]
	v_mfma_f32_16x16x32_f16 v[104:107], v[158:161], v[182:185], v[104:107]
	v_mfma_f32_16x16x32_f16 v[108:111], v[166:169], v[182:185], v[108:111]
	v_mfma_f32_16x16x32_f16 v[88:91], v[158:161], v[190:193], v[88:91]
	v_mfma_f32_16x16x32_f16 v[92:95], v[166:169], v[190:193], v[92:95]
	v_mfma_f32_16x16x32_f16 v[72:75], v[158:161], v[198:201], v[72:75]
	v_mfma_f32_16x16x32_f16 v[76:79], v[166:169], v[198:201], v[76:79]
	s_setprio 0
	s_barrier
	s_add_i32 s65, s51, s42
	v_lshl_add_u64 v[218:219], s[38:39], 0, v[136:137]
	s_mov_b32 m0, s65
	ds_read_b128 v[202:205], v145
	ds_read_b128 v[206:209], v145 offset:1024
	ds_read_b128 v[210:213], v145 offset:2048
	ds_read_b128 v[214:217], v145 offset:3072
	global_load_lds_dwordx4 v[218:219], off
	v_lshl_add_u64 v[220:221], s[38:39], 0, v[134:135]
	s_add_i32 m0, s65, 0x2000
	s_nop 0
	global_load_lds_dwordx4 v[220:221], off
	s_barrier
	s_waitcnt lgkmcnt(0)
	s_setprio 1
	s_waitcnt lgkmcnt(0)
	v_mfma_f32_16x16x32_f16 v[112:115], v[202:205], v[170:173], v[112:115]
	v_mfma_f32_16x16x32_f16 v[116:119], v[210:213], v[170:173], v[116:119]
	v_mfma_f32_16x16x32_f16 v[96:99], v[202:205], v[178:181], v[96:99]
	v_mfma_f32_16x16x32_f16 v[100:103], v[210:213], v[178:181], v[100:103]
	v_mfma_f32_16x16x32_f16 v[80:83], v[202:205], v[186:189], v[80:83]
	v_mfma_f32_16x16x32_f16 v[84:87], v[210:213], v[186:189], v[84:87]
	v_mfma_f32_16x16x32_f16 v[64:67], v[202:205], v[194:197], v[64:67]
	v_mfma_f32_16x16x32_f16 v[68:71], v[210:213], v[194:197], v[68:71]
	v_mfma_f32_16x16x32_f16 v[112:115], v[206:209], v[174:177], v[112:115]
	v_mfma_f32_16x16x32_f16 v[116:119], v[214:217], v[174:177], v[116:119]
	v_mfma_f32_16x16x32_f16 v[96:99], v[206:209], v[182:185], v[96:99]
	v_mfma_f32_16x16x32_f16 v[100:103], v[214:217], v[182:185], v[100:103]
	v_mfma_f32_16x16x32_f16 v[80:83], v[206:209], v[190:193], v[80:83]
	v_mfma_f32_16x16x32_f16 v[84:87], v[214:217], v[190:193], v[84:87]
	v_mfma_f32_16x16x32_f16 v[64:67], v[206:209], v[198:201], v[64:67]
	v_mfma_f32_16x16x32_f16 v[68:71], v[214:217], v[198:201], v[68:71]
	s_setprio 0
	s_mov_b32 m0, s43
	v_lshl_add_u64 v[222:223], s[40:41], 0, v[128:129]
	s_barrier
	ds_read_b128 v[170:173], v143 offset:16384
	ds_read_b128 v[174:177], v143 offset:17408
	ds_read_b128 v[178:181], v143 offset:18432
	ds_read_b128 v[182:185], v143 offset:19456
	ds_read_b128 v[186:189], v143 offset:20480
	ds_read_b128 v[190:193], v143 offset:21504
	ds_read_b128 v[194:197], v143 offset:22528
	ds_read_b128 v[198:201], v143 offset:23552
	global_load_lds_dwordx4 v[222:223], off
	v_lshl_add_u64 v[224:225], v[222:223], 0, s[24:25]
	s_mov_b32 m0, s44
	s_nop 0
	global_load_lds_dwordx4 v[224:225], off
	s_barrier
	s_waitcnt lgkmcnt(0)
	s_setprio 1
	s_waitcnt lgkmcnt(0)
	v_mfma_f32_16x16x32_f16 v[56:59], v[154:157], v[170:173], v[56:59]
	v_mfma_f32_16x16x32_f16 v[60:63], v[162:165], v[170:173], v[60:63]
	v_mfma_f32_16x16x32_f16 v[40:43], v[154:157], v[178:181], v[40:43]
	v_mfma_f32_16x16x32_f16 v[44:47], v[162:165], v[178:181], v[44:47]
	v_mfma_f32_16x16x32_f16 v[24:27], v[154:157], v[186:189], v[24:27]
	v_mfma_f32_16x16x32_f16 v[28:31], v[162:165], v[186:189], v[28:31]
	v_mfma_f32_16x16x32_f16 v[8:11], v[154:157], v[194:197], v[8:11]
	v_mfma_f32_16x16x32_f16 v[12:15], v[162:165], v[194:197], v[12:15]
	v_mfma_f32_16x16x32_f16 v[56:59], v[158:161], v[174:177], v[56:59]
	v_mfma_f32_16x16x32_f16 v[60:63], v[166:169], v[174:177], v[60:63]
	v_mfma_f32_16x16x32_f16 v[40:43], v[158:161], v[182:185], v[40:43]
	v_mfma_f32_16x16x32_f16 v[44:47], v[166:169], v[182:185], v[44:47]
	v_mfma_f32_16x16x32_f16 v[24:27], v[158:161], v[190:193], v[24:27]
	v_mfma_f32_16x16x32_f16 v[28:31], v[166:169], v[190:193], v[28:31]
	v_mfma_f32_16x16x32_f16 v[8:11], v[158:161], v[198:201], v[8:11]
	v_mfma_f32_16x16x32_f16 v[12:15], v[166:169], v[198:201], v[12:15]
	s_setprio 0
	s_barrier
	s_add_u32 s66, s38, 0xb0000
	s_addc_u32 s67, s39, 0
	s_add_i32 s65, s52, s42
	v_lshl_add_u64 v[154:155], s[66:67], 0, v[136:137]
	s_mov_b32 m0, s65
	s_nop 0
	global_load_lds_dwordx4 v[154:155], off
	v_lshl_add_u64 v[154:155], s[66:67], 0, v[134:135]
	s_add_i32 m0, s65, 0x2000
	s_nop 0
	global_load_lds_dwordx4 v[154:155], off
	s_waitcnt vmcnt(6)
	s_barrier
	s_setprio 1
	v_mfma_f32_16x16x32_f16 v[48:51], v[202:205], v[170:173], v[48:51]
	v_mfma_f32_16x16x32_f16 v[52:55], v[210:213], v[170:173], v[52:55]
	v_mfma_f32_16x16x32_f16 v[32:35], v[202:205], v[178:181], v[32:35]
	v_mfma_f32_16x16x32_f16 v[36:39], v[210:213], v[178:181], v[36:39]
	v_mfma_f32_16x16x32_f16 v[16:19], v[202:205], v[186:189], v[16:19]
	v_mfma_f32_16x16x32_f16 v[20:23], v[210:213], v[186:189], v[20:23]
	v_mfma_f32_16x16x32_f16 v[4:7], v[202:205], v[194:197], v[4:7]
	v_mfma_f32_16x16x32_f16 v[0:3], v[210:213], v[194:197], v[0:3]
	v_mfma_f32_16x16x32_f16 v[48:51], v[206:209], v[174:177], v[48:51]
	v_mfma_f32_16x16x32_f16 v[52:55], v[214:217], v[174:177], v[52:55]
	v_mfma_f32_16x16x32_f16 v[32:35], v[206:209], v[182:185], v[32:35]
	v_mfma_f32_16x16x32_f16 v[36:39], v[214:217], v[182:185], v[36:39]
	v_mfma_f32_16x16x32_f16 v[16:19], v[206:209], v[190:193], v[16:19]
	v_mfma_f32_16x16x32_f16 v[20:23], v[214:217], v[190:193], v[20:23]
	v_mfma_f32_16x16x32_f16 v[4:7], v[206:209], v[198:201], v[4:7]
	v_mfma_f32_16x16x32_f16 v[0:3], v[214:217], v[198:201], v[0:3]
	s_setprio 0
	s_add_i32 s65, 0, 0x18000
	v_add_u32_e32 v147, s65, v139
	s_barrier
	ds_read_b128 v[154:157], v147
	ds_read_b128 v[158:161], v147 offset:1024
	ds_read_b128 v[162:165], v147 offset:2048
	ds_read_b128 v[166:169], v147 offset:3072
	s_mov_b32 m0, s45
	v_lshl_add_u64 v[202:203], s[40:41], 0, v[130:131]
	ds_read_b128 v[170:173], v143 offset:32768
	ds_read_b128 v[174:177], v143 offset:33792
	ds_read_b128 v[178:181], v143 offset:34816
	ds_read_b128 v[182:185], v143 offset:35840
	ds_read_b128 v[186:189], v143 offset:36864
	ds_read_b128 v[190:193], v143 offset:37888
	ds_read_b128 v[194:197], v143 offset:38912
	ds_read_b128 v[198:201], v143 offset:39936
	global_load_lds_dwordx4 v[202:203], off
	v_lshl_add_u64 v[202:203], v[222:223], 0, s[26:27]
	s_mov_b32 m0, s46
	s_nop 0
	global_load_lds_dwordx4 v[202:203], off
	s_waitcnt lgkmcnt(8)
	s_barrier
	s_waitcnt lgkmcnt(0)
	s_setprio 1
	s_waitcnt lgkmcnt(0)
	v_mfma_f32_16x16x32_f16 v[120:123], v[154:157], v[170:173], v[120:123]
	v_mfma_f32_16x16x32_f16 v[124:127], v[162:165], v[170:173], v[124:127]
	v_mfma_f32_16x16x32_f16 v[104:107], v[154:157], v[178:181], v[104:107]
	v_mfma_f32_16x16x32_f16 v[108:111], v[162:165], v[178:181], v[108:111]
	v_mfma_f32_16x16x32_f16 v[88:91], v[154:157], v[186:189], v[88:91]
	v_mfma_f32_16x16x32_f16 v[92:95], v[162:165], v[186:189], v[92:95]
	v_mfma_f32_16x16x32_f16 v[72:75], v[154:157], v[194:197], v[72:75]
	v_mfma_f32_16x16x32_f16 v[76:79], v[162:165], v[194:197], v[76:79]
	v_mfma_f32_16x16x32_f16 v[120:123], v[158:161], v[174:177], v[120:123]
	v_mfma_f32_16x16x32_f16 v[124:127], v[166:169], v[174:177], v[124:127]
	v_mfma_f32_16x16x32_f16 v[104:107], v[158:161], v[182:185], v[104:107]
	v_mfma_f32_16x16x32_f16 v[108:111], v[166:169], v[182:185], v[108:111]
	v_mfma_f32_16x16x32_f16 v[88:91], v[158:161], v[190:193], v[88:91]
	v_mfma_f32_16x16x32_f16 v[92:95], v[166:169], v[190:193], v[92:95]
	v_mfma_f32_16x16x32_f16 v[72:75], v[158:161], v[198:201], v[72:75]
	v_mfma_f32_16x16x32_f16 v[76:79], v[166:169], v[198:201], v[76:79]
	s_setprio 0
	s_barrier
	s_add_i32 s40, 0, 0x1c000
	s_add_i32 s41, s65, s42
	v_add_u32_e32 v147, s40, v139
	v_lshl_add_u64 v[218:219], v[218:219], 0, s[4:5]
	s_mov_b32 m0, s41
	ds_read_b128 v[202:205], v147
	ds_read_b128 v[206:209], v147 offset:1024
	ds_read_b128 v[210:213], v147 offset:2048
	ds_read_b128 v[214:217], v147 offset:3072
	global_load_lds_dwordx4 v[218:219], off
	v_lshl_add_u64 v[218:219], v[220:221], 0, s[4:5]
	s_add_i32 m0, s41, 0x2000
	s_nop 0
	global_load_lds_dwordx4 v[218:219], off
	s_barrier
	s_waitcnt lgkmcnt(0)
	s_setprio 1
	s_waitcnt lgkmcnt(0)
	v_mfma_f32_16x16x32_f16 v[112:115], v[202:205], v[170:173], v[112:115]
	v_mfma_f32_16x16x32_f16 v[116:119], v[210:213], v[170:173], v[116:119]
	v_mfma_f32_16x16x32_f16 v[96:99], v[202:205], v[178:181], v[96:99]
	v_mfma_f32_16x16x32_f16 v[100:103], v[210:213], v[178:181], v[100:103]
	v_mfma_f32_16x16x32_f16 v[80:83], v[202:205], v[186:189], v[80:83]
	v_mfma_f32_16x16x32_f16 v[84:87], v[210:213], v[186:189], v[84:87]
	v_mfma_f32_16x16x32_f16 v[64:67], v[202:205], v[194:197], v[64:67]
	v_mfma_f32_16x16x32_f16 v[68:71], v[210:213], v[194:197], v[68:71]
	v_mfma_f32_16x16x32_f16 v[112:115], v[206:209], v[174:177], v[112:115]
	v_mfma_f32_16x16x32_f16 v[116:119], v[214:217], v[174:177], v[116:119]
	v_mfma_f32_16x16x32_f16 v[96:99], v[206:209], v[182:185], v[96:99]
	v_mfma_f32_16x16x32_f16 v[100:103], v[214:217], v[182:185], v[100:103]
	v_mfma_f32_16x16x32_f16 v[80:83], v[206:209], v[190:193], v[80:83]
	v_mfma_f32_16x16x32_f16 v[84:87], v[214:217], v[190:193], v[84:87]
	v_mfma_f32_16x16x32_f16 v[64:67], v[206:209], v[198:201], v[64:67]
	v_mfma_f32_16x16x32_f16 v[68:71], v[214:217], v[198:201], v[68:71]
	s_setprio 0
	s_mov_b32 m0, s47
	v_lshl_add_u64 v[218:219], v[222:223], 0, s[18:19]
	s_barrier
	ds_read_b128 v[170:173], v143 offset:49152
	ds_read_b128 v[174:177], v143 offset:50176
	ds_read_b128 v[178:181], v143 offset:51200
	ds_read_b128 v[182:185], v143 offset:52224
	ds_read_b128 v[186:189], v143 offset:53248
	ds_read_b128 v[190:193], v143 offset:54272
	ds_read_b128 v[194:197], v143 offset:55296
	ds_read_b128 v[198:201], v143 offset:56320
	global_load_lds_dwordx4 v[218:219], off
	v_lshl_add_u64 v[218:219], v[222:223], 0, s[28:29]
	s_mov_b32 m0, s48
	s_nop 0
	global_load_lds_dwordx4 v[218:219], off
	s_barrier
	s_waitcnt lgkmcnt(0)
	s_setprio 1
	s_waitcnt lgkmcnt(0)
	v_mfma_f32_16x16x32_f16 v[56:59], v[154:157], v[170:173], v[56:59]
	v_mfma_f32_16x16x32_f16 v[60:63], v[162:165], v[170:173], v[60:63]
	v_mfma_f32_16x16x32_f16 v[40:43], v[154:157], v[178:181], v[40:43]
	v_mfma_f32_16x16x32_f16 v[44:47], v[162:165], v[178:181], v[44:47]
	v_mfma_f32_16x16x32_f16 v[24:27], v[154:157], v[186:189], v[24:27]
	v_mfma_f32_16x16x32_f16 v[28:31], v[162:165], v[186:189], v[28:31]
	v_mfma_f32_16x16x32_f16 v[8:11], v[154:157], v[194:197], v[8:11]
	v_mfma_f32_16x16x32_f16 v[12:15], v[162:165], v[194:197], v[12:15]
	v_mfma_f32_16x16x32_f16 v[56:59], v[158:161], v[174:177], v[56:59]
	v_mfma_f32_16x16x32_f16 v[60:63], v[166:169], v[174:177], v[60:63]
	v_mfma_f32_16x16x32_f16 v[40:43], v[158:161], v[182:185], v[40:43]
	v_mfma_f32_16x16x32_f16 v[44:47], v[166:169], v[182:185], v[44:47]
	v_mfma_f32_16x16x32_f16 v[24:27], v[158:161], v[190:193], v[24:27]
	v_mfma_f32_16x16x32_f16 v[28:31], v[166:169], v[190:193], v[28:31]
	v_mfma_f32_16x16x32_f16 v[8:11], v[158:161], v[198:201], v[8:11]
	v_mfma_f32_16x16x32_f16 v[12:15], v[166:169], v[198:201], v[12:15]
	s_setprio 0
	s_barrier
	s_add_u32 s38, s38, 0xb0080
	s_addc_u32 s39, s39, 0
	s_add_i32 s40, s40, s42
	v_lshl_add_u64 v[154:155], s[38:39], 0, v[136:137]
	s_mov_b32 m0, s40
	s_nop 0
	global_load_lds_dwordx4 v[154:155], off
	v_lshl_add_u64 v[154:155], s[38:39], 0, v[134:135]
	s_add_i32 m0, s40, 0x2000
	s_nop 0
	global_load_lds_dwordx4 v[154:155], off
	s_add_u32 s62, s62, 0x100
	s_addc_u32 s63, s63, 0
	s_add_u32 s36, s36, 0x10000
	s_addc_u32 s37, s37, 0
	s_waitcnt vmcnt(6)
	s_barrier
	s_setprio 1
	v_mfma_f32_16x16x32_f16 v[48:51], v[202:205], v[170:173], v[48:51]
	v_mfma_f32_16x16x32_f16 v[52:55], v[210:213], v[170:173], v[52:55]
	v_mfma_f32_16x16x32_f16 v[32:35], v[202:205], v[178:181], v[32:35]
	v_mfma_f32_16x16x32_f16 v[36:39], v[210:213], v[178:181], v[36:39]
	v_mfma_f32_16x16x32_f16 v[16:19], v[202:205], v[186:189], v[16:19]
	v_mfma_f32_16x16x32_f16 v[20:23], v[210:213], v[186:189], v[20:23]
	v_mfma_f32_16x16x32_f16 v[4:7], v[202:205], v[194:197], v[4:7]
	v_mfma_f32_16x16x32_f16 v[0:3], v[210:213], v[194:197], v[0:3]
	v_mfma_f32_16x16x32_f16 v[48:51], v[206:209], v[174:177], v[48:51]
	v_mfma_f32_16x16x32_f16 v[52:55], v[214:217], v[174:177], v[52:55]
	v_mfma_f32_16x16x32_f16 v[32:35], v[206:209], v[182:185], v[32:35]
	v_mfma_f32_16x16x32_f16 v[36:39], v[214:217], v[182:185], v[36:39]
	v_mfma_f32_16x16x32_f16 v[16:19], v[206:209], v[190:193], v[16:19]
	v_mfma_f32_16x16x32_f16 v[20:23], v[214:217], v[190:193], v[20:23]
	v_mfma_f32_16x16x32_f16 v[4:7], v[206:209], v[198:201], v[4:7]
	v_mfma_f32_16x16x32_f16 v[0:3], v[214:217], v[198:201], v[0:3]
	s_setprio 0
	s_cmp_ge_i32 s64, s61
	s_mov_b32 s38, s64
	s_barrier
	s_cbranch_scc0 .LBB2_13
	s_cmp_lg_u32 s16, 0
	s_cbranch_scc0 .LBB2_17

.LBB4_46:
	s_mov_b32 m0, s67
	v_lshl_add_u64 v[182:183], v[182:183], 0, s[30:31]
	ds_read_b128 v[190:193], v238
	ds_read_b128 v[194:197], v238 offset:1024
	ds_read_b128 v[198:201], v238 offset:2048
	ds_read_b128 v[202:205], v238 offset:3072
	global_load_lds_dwordx4 v[182:183], off
	v_lshl_add_u64 v[182:183], v[184:185], 0, s[30:31]
	s_mov_b32 m0, s68
	v_mov_b32_e32 v227, v221
	global_load_lds_dwordx4 v[182:183], off
	s_barrier
	s_waitcnt lgkmcnt(0)
	v_lshl_add_u64 v[186:187], s[48:49], 0, v[220:221]
	v_lshl_add_u64 v[188:189], s[48:49], 0, v[226:227]
	s_setprio 1
	s_waitcnt lgkmcnt(0)
	v_mfma_f32_16x16x32_f16 v[130:133], v[190:193], v[174:177], v[130:133]
	v_mfma_f32_16x16x32_f16 v[126:129], v[198:201], v[174:177], v[126:129]
	v_mfma_f32_16x16x32_f16 v[122:125], v[190:193], v[166:169], v[122:125]
	v_mfma_f32_16x16x32_f16 v[118:121], v[198:201], v[166:169], v[118:121]
	v_mfma_f32_16x16x32_f16 v[110:113], v[190:193], v[158:161], v[110:113]
	v_mfma_f32_16x16x32_f16 v[102:105], v[198:201], v[158:161], v[102:105]
	v_mfma_f32_16x16x32_f16 v[94:97], v[190:193], v[150:153], v[94:97]
	v_mfma_f32_16x16x32_f16 v[82:85], v[198:201], v[150:153], v[82:85]
	v_mfma_f32_16x16x32_f16 v[130:133], v[194:197], v[178:181], v[130:133]
	v_mfma_f32_16x16x32_f16 v[126:129], v[202:205], v[178:181], v[126:129]
	v_mfma_f32_16x16x32_f16 v[122:125], v[194:197], v[170:173], v[122:125]
	v_mfma_f32_16x16x32_f16 v[118:121], v[202:205], v[170:173], v[118:121]
	v_mfma_f32_16x16x32_f16 v[110:113], v[194:197], v[162:165], v[110:113]
	v_mfma_f32_16x16x32_f16 v[102:105], v[202:205], v[162:165], v[102:105]
	v_mfma_f32_16x16x32_f16 v[94:97], v[194:197], v[154:157], v[94:97]
	v_mfma_f32_16x16x32_f16 v[82:85], v[202:205], v[154:157], v[82:85]
	s_setprio 0
	s_mov_b32 m0, s69
	v_lshl_add_u64 v[182:183], v[186:187], 0, s[30:31]
	s_barrier
	ds_read_b128 v[150:153], v237 offset:49152
	ds_read_b128 v[154:157], v237 offset:50176
	ds_read_b128 v[158:161], v237 offset:51200
	ds_read_b128 v[162:165], v237 offset:52224
	ds_read_b128 v[166:169], v237 offset:53248
	ds_read_b128 v[170:173], v237 offset:54272
	ds_read_b128 v[174:177], v237 offset:55296
	ds_read_b128 v[178:181], v237 offset:56320
	global_load_lds_dwordx4 v[182:183], off
	v_lshl_add_u64 v[182:183], v[188:189], 0, s[30:31]
	s_mov_b32 m0, s70
	s_nop 0
	global_load_lds_dwordx4 v[182:183], off
	s_barrier
	s_waitcnt lgkmcnt(0)
	s_setprio 1
	s_waitcnt lgkmcnt(0)
	v_mfma_f32_16x16x32_f16 v[70:73], v[134:137], v[150:153], v[70:73]
	v_mfma_f32_16x16x32_f16 v[58:61], v[142:145], v[150:153], v[58:61]
	v_mfma_f32_16x16x32_f16 v[50:53], v[134:137], v[158:161], v[50:53]
	v_mfma_f32_16x16x32_f16 v[38:41], v[142:145], v[158:161], v[38:41]
	v_mfma_f32_16x16x32_f16 v[26:29], v[134:137], v[166:169], v[26:29]
	v_mfma_f32_16x16x32_f16 v[18:21], v[142:145], v[166:169], v[18:21]
	v_mfma_f32_16x16x32_f16 v[10:13], v[134:137], v[174:177], v[10:13]
	v_mfma_f32_16x16x32_f16 v[6:9], v[142:145], v[174:177], v[6:9]
	v_mfma_f32_16x16x32_f16 v[70:73], v[138:141], v[154:157], v[70:73]
	v_mfma_f32_16x16x32_f16 v[58:61], v[146:149], v[154:157], v[58:61]
	v_mfma_f32_16x16x32_f16 v[50:53], v[138:141], v[162:165], v[50:53]
	v_mfma_f32_16x16x32_f16 v[38:41], v[146:149], v[162:165], v[38:41]
	v_mfma_f32_16x16x32_f16 v[26:29], v[138:141], v[170:173], v[26:29]
	v_mfma_f32_16x16x32_f16 v[18:21], v[146:149], v[170:173], v[18:21]
	v_mfma_f32_16x16x32_f16 v[10:13], v[138:141], v[178:181], v[10:13]
	v_mfma_f32_16x16x32_f16 v[6:9], v[146:149], v[178:181], v[6:9]
	s_setprio 0
	s_barrier
	s_add_u32 s44, s44, 0x40080
	s_addc_u32 s45, s45, 0
	s_mov_b32 m0, s50
	v_lshl_add_u64 v[134:135], s[44:45], 0, v[216:217]
	global_load_lds_dwordx4 v[134:135], off
	v_lshl_add_u64 v[134:135], s[44:45], 0, v[218:219]
	s_mov_b32 m0, s51
	s_nop 0
	global_load_lds_dwordx4 v[134:135], off
	s_add_i32 s94, s61, s33
	s_mov_b32 s95, 0
	s_cmpk_gt_u32 s94, 0x15ff
	s_cselect_b64 s[96:97], -1, 0
	s_and_b64 s[96:97], s[96:97], exec
	s_cselect_b32 s96, 0x7fffea00, 0
	s_cselect_b32 s98, s25, s15
	s_cselect_b32 s99, s24, s14
	s_add_i32 s96, s96, s94
	s_lshl_b32 s94, s96, 1
	s_addk_i32 s94, 0x2c00
	s_lshl_b64 s[96:97], s[94:95], 12
	s_add_u32 s100, s99, s96
	s_addc_u32 s101, s98, s97
	s_add_i32 s94, s75, s61
	s_cmpk_gt_u32 s94, 0x15ff
	s_cselect_b32 s97, 0x7fffea00, 0
	s_cselect_b32 s96, 0x80, 0
	s_add_i32 s97, s97, s94
	s_lshl_b32 s94, s97, 1
	s_add_i32 s97, s94, 0x2c00
	s_mul_hi_u32 s98, s97, 0xba2e8ba3
	s_lshr_b32 s98, s98, 11
	s_mul_i32 s99, s98, 0x7ffff500
	s_add_i32 s99, s99, s97
	s_lshr_b32 s97, s99, 7
	s_mul_i32 s98, s98, 22
	s_add_i32 s97, s97, s98
	s_lshl_b32 s97, s97, 8
	s_and_b32 s94, s94, 0x7e
	s_or_b32 s96, s97, s96
	s_or_b32 s94, s96, s94
	s_lshl_b64 s[96:97], s[94:95], 11
	s_add_i32 s28, s88, 2
	s_add_u32 s46, s46, 0x100
	s_addc_u32 s47, s47, 0
	s_add_u32 s86, s86, 0x100
	s_addc_u32 s87, s87, 0
	s_waitcnt vmcnt(6)
	s_cmp_gt_i32 s61, 44
	s_cbranch_scc1 .Lhka_done_a3
	s_cmp_lt_i32 s61, 1
	s_cbranch_scc1 .Lhka_ld_a3
	v_cvt_pk_f16_f32 v2, v2, v3
	v_cvt_pk_f16_f32 v3, v4, v5
	v_lshl_add_u64 v[4:5], v[224:225], 0, s[96:97]
	global_store_dwordx2 v[4:5], v[2:3], off

.Lhka_done_a3:
	s_barrier
	s_setprio 1
	v_mfma_f32_16x16x32_f16 v[90:93], v[190:193], v[150:153], v[90:93]
	v_mfma_f32_16x16x32_f16 v[78:81], v[198:201], v[150:153], v[78:81]
	v_mfma_f32_16x16x32_f16 v[66:69], v[190:193], v[158:161], v[66:69]
	v_mfma_f32_16x16x32_f16 v[54:57], v[198:201], v[158:161], v[54:57]
	v_mfma_f32_16x16x32_f16 v[42:45], v[190:193], v[166:169], v[42:45]
	v_mfma_f32_16x16x32_f16 v[30:33], v[198:201], v[166:169], v[30:33]
	v_mfma_f32_16x16x32_f16 v[22:25], v[190:193], v[174:177], v[22:25]
	v_mfma_f32_16x16x32_f16 v[14:17], v[198:201], v[174:177], v[14:17]
	v_mfma_f32_16x16x32_f16 v[90:93], v[194:197], v[154:157], v[90:93]
	v_mfma_f32_16x16x32_f16 v[78:81], v[202:205], v[154:157], v[78:81]
	v_mfma_f32_16x16x32_f16 v[66:69], v[194:197], v[162:165], v[66:69]
	v_mfma_f32_16x16x32_f16 v[54:57], v[202:205], v[162:165], v[54:57]
	v_mfma_f32_16x16x32_f16 v[42:45], v[194:197], v[170:173], v[42:45]
	v_mfma_f32_16x16x32_f16 v[30:33], v[202:205], v[170:173], v[30:33]
	v_mfma_f32_16x16x32_f16 v[22:25], v[194:197], v[178:181], v[22:25]
	v_mfma_f32_16x16x32_f16 v[14:17], v[202:205], v[178:181], v[14:17]
	s_setprio 0
	s_cmp_ge_i32 s88, s83
	s_barrier
	s_cbranch_scc1 .LBB4_49
	s_mov_b32 s88, s28
	s_branch .LBB4_32

.LBB5_46:
	s_mov_b32 m0, s62
	v_lshl_add_u64 v[182:183], v[182:183], 0, s[26:27]
	ds_read_b128 v[190:193], v236
	ds_read_b128 v[194:197], v236 offset:1024
	ds_read_b128 v[198:201], v236 offset:2048
	ds_read_b128 v[202:205], v236 offset:3072
	global_load_lds_dwordx4 v[182:183], off
	v_lshl_add_u64 v[182:183], v[184:185], 0, s[26:27]
	s_mov_b32 m0, s64
	v_mov_b32_e32 v223, v217
	global_load_lds_dwordx4 v[182:183], off
	s_barrier
	s_waitcnt lgkmcnt(0)
	v_lshl_add_u64 v[186:187], s[44:45], 0, v[216:217]
	v_lshl_add_u64 v[188:189], s[44:45], 0, v[222:223]
	s_setprio 1
	s_waitcnt lgkmcnt(0)
	v_mfma_f32_16x16x32_f16 v[130:133], v[190:193], v[174:177], v[130:133]
	v_mfma_f32_16x16x32_f16 v[126:129], v[198:201], v[174:177], v[126:129]
	v_mfma_f32_16x16x32_f16 v[122:125], v[190:193], v[166:169], v[122:125]
	v_mfma_f32_16x16x32_f16 v[114:117], v[198:201], v[166:169], v[114:117]
	v_mfma_f32_16x16x32_f16 v[106:109], v[190:193], v[158:161], v[106:109]
	v_mfma_f32_16x16x32_f16 v[98:101], v[198:201], v[158:161], v[98:101]
	v_mfma_f32_16x16x32_f16 v[90:93], v[190:193], v[150:153], v[90:93]
	v_mfma_f32_16x16x32_f16 v[78:81], v[198:201], v[150:153], v[78:81]
	v_mfma_f32_16x16x32_f16 v[130:133], v[194:197], v[178:181], v[130:133]
	v_mfma_f32_16x16x32_f16 v[126:129], v[202:205], v[178:181], v[126:129]
	v_mfma_f32_16x16x32_f16 v[122:125], v[194:197], v[170:173], v[122:125]
	v_mfma_f32_16x16x32_f16 v[114:117], v[202:205], v[170:173], v[114:117]
	v_mfma_f32_16x16x32_f16 v[106:109], v[194:197], v[162:165], v[106:109]
	v_mfma_f32_16x16x32_f16 v[98:101], v[202:205], v[162:165], v[98:101]
	v_mfma_f32_16x16x32_f16 v[90:93], v[194:197], v[154:157], v[90:93]
	v_mfma_f32_16x16x32_f16 v[78:81], v[202:205], v[154:157], v[78:81]
	s_setprio 0
	s_mov_b32 m0, s65
	v_lshl_add_u64 v[182:183], v[186:187], 0, s[26:27]
	s_barrier
	ds_read_b128 v[150:153], v235 offset:49152
	ds_read_b128 v[154:157], v235 offset:50176
	ds_read_b128 v[158:161], v235 offset:51200
	ds_read_b128 v[162:165], v235 offset:52224
	ds_read_b128 v[166:169], v235 offset:53248
	ds_read_b128 v[170:173], v235 offset:54272
	ds_read_b128 v[174:177], v235 offset:55296
	ds_read_b128 v[178:181], v235 offset:56320
	global_load_lds_dwordx4 v[182:183], off
	v_lshl_add_u64 v[182:183], v[188:189], 0, s[26:27]
	s_mov_b32 m0, s66
	s_nop 0
	global_load_lds_dwordx4 v[182:183], off
	s_barrier
	s_waitcnt lgkmcnt(0)
	s_setprio 1
	s_waitcnt lgkmcnt(0)
	v_mfma_f32_16x16x32_f16 v[70:73], v[134:137], v[150:153], v[70:73]
	v_mfma_f32_16x16x32_f16 v[58:61], v[142:145], v[150:153], v[58:61]
	v_mfma_f32_16x16x32_f16 v[46:49], v[134:137], v[158:161], v[46:49]
	v_mfma_f32_16x16x32_f16 v[34:37], v[142:145], v[158:161], v[34:37]
	v_mfma_f32_16x16x32_f16 v[26:29], v[134:137], v[166:169], v[26:29]
	v_mfma_f32_16x16x32_f16 v[18:21], v[142:145], v[166:169], v[18:21]
	v_mfma_f32_16x16x32_f16 v[10:13], v[134:137], v[174:177], v[10:13]
	v_mfma_f32_16x16x32_f16 v[6:9], v[142:145], v[174:177], v[6:9]
	v_mfma_f32_16x16x32_f16 v[70:73], v[138:141], v[154:157], v[70:73]
	v_mfma_f32_16x16x32_f16 v[58:61], v[146:149], v[154:157], v[58:61]
	v_mfma_f32_16x16x32_f16 v[46:49], v[138:141], v[162:165], v[46:49]
	v_mfma_f32_16x16x32_f16 v[34:37], v[146:149], v[162:165], v[34:37]
	v_mfma_f32_16x16x32_f16 v[26:29], v[138:141], v[170:173], v[26:29]
	v_mfma_f32_16x16x32_f16 v[18:21], v[146:149], v[170:173], v[18:21]
	v_mfma_f32_16x16x32_f16 v[10:13], v[138:141], v[178:181], v[10:13]
	v_mfma_f32_16x16x32_f16 v[6:9], v[146:149], v[178:181], v[6:9]
	s_setprio 0
	s_barrier
	s_add_u32 s40, s40, 0x40080
	s_addc_u32 s41, s41, 0
	s_mov_b32 m0, s46
	v_lshl_add_u64 v[134:135], s[40:41], 0, v[212:213]
	global_load_lds_dwordx4 v[134:135], off
	v_lshl_add_u64 v[134:135], s[40:41], 0, v[214:215]
	s_mov_b32 m0, s47
	s_nop 0
	global_load_lds_dwordx4 v[134:135], off
	s_add_i32 s92, s71, s63
	s_mov_b32 s93, 0
	s_lshl_b64 s[90:91], s[92:93], 12
	s_add_i32 s92, s63, s33
	s_lshl_b64 s[92:93], s[92:93], 13
	s_add_i32 s24, s84, 2
	s_add_u32 s42, s42, 0x100
	s_addc_u32 s43, s43, 0
	s_add_u32 s82, s82, 0x100
	s_addc_u32 s83, s83, 0
	s_waitcnt vmcnt(6)
	s_cmp_gt_i32 s63, 44
	s_cbranch_scc1 .Lhkb_done_b3
	s_cmp_lt_i32 s63, 1
	s_cbranch_scc1 .Lhkb_ld_b3
	v_cvt_pk_f16_f32 v2, v2, v3
	v_cvt_pk_f16_f32 v3, v4, v5
	v_lshl_add_u64 v[4:5], v[220:221], 0, s[90:91]
	global_store_dwordx2 v[4:5], v[2:3], off

.Lhkb_done_b3:
	s_barrier
	s_setprio 1
	v_mfma_f32_16x16x32_f16 v[86:89], v[190:193], v[150:153], v[86:89]
	v_mfma_f32_16x16x32_f16 v[74:77], v[198:201], v[150:153], v[74:77]
	v_mfma_f32_16x16x32_f16 v[62:65], v[190:193], v[158:161], v[62:65]
	v_mfma_f32_16x16x32_f16 v[50:53], v[198:201], v[158:161], v[50:53]
	v_mfma_f32_16x16x32_f16 v[38:41], v[190:193], v[166:169], v[38:41]
	v_mfma_f32_16x16x32_f16 v[30:33], v[198:201], v[166:169], v[30:33]
	v_mfma_f32_16x16x32_f16 v[22:25], v[190:193], v[174:177], v[22:25]
	v_mfma_f32_16x16x32_f16 v[14:17], v[198:201], v[174:177], v[14:17]
	v_mfma_f32_16x16x32_f16 v[86:89], v[194:197], v[154:157], v[86:89]
	v_mfma_f32_16x16x32_f16 v[74:77], v[202:205], v[154:157], v[74:77]
	v_mfma_f32_16x16x32_f16 v[62:65], v[194:197], v[162:165], v[62:65]
	v_mfma_f32_16x16x32_f16 v[50:53], v[202:205], v[162:165], v[50:53]
	v_mfma_f32_16x16x32_f16 v[38:41], v[194:197], v[170:173], v[38:41]
	v_mfma_f32_16x16x32_f16 v[30:33], v[202:205], v[170:173], v[30:33]
	v_mfma_f32_16x16x32_f16 v[22:25], v[194:197], v[178:181], v[22:25]
	v_mfma_f32_16x16x32_f16 v[14:17], v[202:205], v[178:181], v[14:17]
	s_setprio 0
	s_cmp_ge_i32 s84, s79
	s_barrier
	s_cbranch_scc1 .LBB5_49
	s_mov_b32 s84, s24
	s_branch .LBB5_32
